# P1 epilogue duplicated: write-back stores for tiles 0-4, write-through (sc1) only for the last tile
# baseline (speedup 1.0000x reference)
; __device__ __forceinline__ unsigned cvt_pk_bf16(float lo, float hi) { unsigned r; asm volatile("v_cvt_pk_bf16_f32 %0, %1, %2" : "=v"(r) : "v"(lo), "v"(hi)); return r; }
;     __device__ __forceinline__ void operator()(const f32x4 (&acc)[2][2][4][2], const Unit& u, int wr, int wc, int fr, int fq) const {
;         const int row0 = u.pm * BM + wr * 64 + fr, col0 = u.pn * BM + wc * 32 + 8 * fq;
; #pragma unroll
;         for (int bj = 0; bj < 2; ++bj) {
;             const f32x4 s0 = *(const f32x4*)(sb + col0 + bj * HALF), s1 = *(const f32x4*)(sb + col0 + bj * HALF + 4);
; #pragma unroll
;             for (int ai = 0; ai < 2; ++ai)
; #pragma unroll
;                 for (int m = 0; m < 4; ++m) { const int row = row0 + ai * HALF + m * 16; bf16_t* rowp = O + (size_t)row * ldc + col0 + bj * HALF;
;                     f32x4 v0, v1;
;                     if constexpr (I8) { const float ra = sa[row]; const i32x4 i0 = __builtin_bit_cast(i32x4, acc[ai][bj][m][0]), i1 = __builtin_bit_cast(i32x4, acc[ai][bj][m][1]);
;                         v0 = __builtin_convertvector(i0, f32x4) * ra * s0; v1 = __builtin_convertvector(i1, f32x4) * ra * s1; }
;                     else { v0 = acc[ai][bj][m][0] * s0; v1 = acc[ai][bj][m][1] * s1; }
;                     u32x4 w; w.x = cvt_pk_bf16(v0[0], v0[1]); w.y = cvt_pk_bf16(v0[2], v0[3]); w.z = cvt_pk_bf16(v1[0], v1[1]); w.w = cvt_pk_bf16(v1[2], v1[3]);
;                     *(u32x4*)rowp = w; }
.LBB0_150:
	s_and_b64 vcc, exec, s[38:39]
	s_cbranch_vccz .Lmy_p1epi_last
	v_lshl_add_u32 v152, s84, 8, v160
	v_lshl_or_b32 v146, s85, 8, v161
	v_ashrrev_i32_e32 v147, 31, v146
	v_ashrrev_i32_e32 v153, 31, v152
	v_lshl_add_u64 v[150:151], v[146:147], 2, s[40:41]
	v_lshlrev_b64 v[156:157], 1, v[146:147]
	v_lshl_add_u64 v[146:147], v[152:153], 2, s[46:47]
	global_load_dwordx4 v[122:125], v[150:151], off offset:16
	global_load_dwordx4 v[126:129], v[150:151], off
	global_load_dword v164, v[146:147], off
	global_load_dword v180, v[146:147], off offset:64
	global_load_dword v182, v[146:147], off offset:128
	global_load_dword v184, v[146:147], off offset:192
	global_load_dword v186, v[146:147], off offset:512
	global_load_dword v188, v[146:147], off offset:576
	global_load_dword v190, v[146:147], off offset:640
	global_load_dword v192, v[146:147], off offset:704
	global_load_dword v178, v[146:147], off
	global_load_dwordx4 v[194:197], v[150:151], off offset:528
	global_load_dwordx4 v[198:201], v[150:151], off offset:512
	v_cvt_f32_i32_e32 v133, v133
	v_cvt_f32_i32_e32 v132, v132
	v_cvt_f32_i32_e32 v131, v131
	v_cvt_f32_i32_e32 v130, v130
	v_cvt_f32_i32_e32 v137, v137
	v_cvt_f32_i32_e32 v136, v136
	v_cvt_f32_i32_e32 v135, v135
	v_cvt_f32_i32_e32 v134, v134
	v_mov_b64_e32 v[154:155], s[74:75]
	v_mad_i64_i32 v[148:149], s[6:7], v152, s63, v[154:155]
	v_lshl_add_u64 v[148:149], v[148:149], 0, v[156:157]
	v_cvt_f32_i32_e32 v117, v117
	v_cvt_f32_i32_e32 v116, v116
	v_cvt_f32_i32_e32 v115, v115
	v_cvt_f32_i32_e32 v114, v114
	v_cvt_f32_i32_e32 v121, v121
	v_cvt_f32_i32_e32 v120, v120
	v_cvt_f32_i32_e32 v119, v119
	v_cvt_f32_i32_e32 v118, v118
	v_cvt_f32_i32_e32 v109, v109
	v_cvt_f32_i32_e32 v108, v108
	v_cvt_f32_i32_e32 v107, v107
	v_cvt_f32_i32_e32 v106, v106
	v_cvt_f32_i32_e32 v113, v113
	v_cvt_f32_i32_e32 v112, v112
	v_cvt_f32_i32_e32 v111, v111
	v_cvt_f32_i32_e32 v110, v110
	v_cvt_f32_i32_e32 v101, v101
	v_cvt_f32_i32_e32 v100, v100
	v_cvt_f32_i32_e32 v99, v99
	v_cvt_f32_i32_e32 v98, v98
	v_cvt_f32_i32_e32 v105, v105
	v_cvt_f32_i32_e32 v104, v104
	v_cvt_f32_i32_e32 v103, v103
	v_cvt_f32_i32_e32 v102, v102
	v_cvt_f32_i32_e32 v93, v93
	v_cvt_f32_i32_e32 v92, v92
	v_cvt_f32_i32_e32 v91, v91
	v_cvt_f32_i32_e32 v90, v90
	v_cvt_f32_i32_e32 v97, v97
	v_cvt_f32_i32_e32 v96, v96
	v_cvt_f32_i32_e32 v95, v95
	v_cvt_f32_i32_e32 v94, v94
	v_cvt_f32_i32_e32 v85, v85
	v_cvt_f32_i32_e32 v84, v84
	v_cvt_f32_i32_e32 v83, v83
	v_cvt_f32_i32_e32 v82, v82
	v_cvt_f32_i32_e32 v89, v89
	v_cvt_f32_i32_e32 v88, v88
	v_cvt_f32_i32_e32 v87, v87
	v_cvt_f32_i32_e32 v86, v86
	v_cvt_f32_i32_e32 v77, v77
	v_cvt_f32_i32_e32 v76, v76
	v_cvt_f32_i32_e32 v75, v75
	v_cvt_f32_i32_e32 v74, v74
	v_cvt_f32_i32_e32 v81, v81
	v_cvt_f32_i32_e32 v80, v80
	v_cvt_f32_i32_e32 v79, v79
	v_cvt_f32_i32_e32 v78, v78
	v_cvt_f32_i32_e32 v69, v69
	v_cvt_f32_i32_e32 v68, v68
	v_cvt_f32_i32_e32 v67, v67
	v_cvt_f32_i32_e32 v66, v66
	v_cvt_f32_i32_e32 v73, v73
	v_cvt_f32_i32_e32 v72, v72
	v_cvt_f32_i32_e32 v71, v71
	v_cvt_f32_i32_e32 v70, v70
	v_cvt_f32_i32_e32 v61, v61
	v_cvt_f32_i32_e32 v60, v60
	v_cvt_f32_i32_e32 v59, v59
	v_cvt_f32_i32_e32 v58, v58
	v_cvt_f32_i32_e32 v65, v65
	v_cvt_f32_i32_e32 v64, v64
	v_cvt_f32_i32_e32 v63, v63
	v_cvt_f32_i32_e32 v62, v62
	v_cvt_f32_i32_e32 v53, v53
	v_cvt_f32_i32_e32 v52, v52
	v_cvt_f32_i32_e32 v51, v51
	s_waitcnt vmcnt(0)
	v_pk_mul_f32 v[130:131], v[164:165], v[130:131] op_sel_hi:[0,1]
	v_pk_mul_f32 v[132:133], v[164:165], v[132:133] op_sel_hi:[0,1]
	v_pk_mul_f32 v[134:135], v[164:165], v[134:135] op_sel_hi:[0,1]
	v_pk_mul_f32 v[136:137], v[164:165], v[136:137] op_sel_hi:[0,1]
	v_pk_mul_f32 v[164:165], v[124:125], v[132:133]
	v_pk_mul_f32 v[132:133], v[122:123], v[130:131]
	v_pk_mul_f32 v[136:137], v[128:129], v[136:137]
	v_pk_mul_f32 v[134:135], v[126:127], v[134:135]
	v_cvt_f32_i32_e32 v50, v50
	v_cvt_pk_bf16_f32 v130, v134, v135
	v_cvt_pk_bf16_f32 v131, v136, v137
	v_cvt_pk_bf16_f32 v132, v132, v133
	v_cvt_pk_bf16_f32 v133, v164, v165
	global_store_dwordx4 v[148:149], v[130:133], off
	v_cvt_f32_i32_e32 v57, v57
	v_cvt_f32_i32_e32 v56, v56
	v_or_b32_e32 v132, 16, v152
	v_ashrrev_i32_e32 v133, 31, v132
	v_mad_i64_i32 v[130:131], s[6:7], v132, s63, v[154:155]
	v_lshl_add_u64 v[132:133], v[132:133], 2, s[46:47]
	s_nop 1
	v_lshl_add_u64 v[130:131], v[130:131], 0, v[156:157]
	v_cvt_f32_i32_e32 v55, v55
	v_cvt_f32_i32_e32 v54, v54
	v_cvt_f32_i32_e32 v45, v45
	v_cvt_f32_i32_e32 v44, v44
	v_cvt_f32_i32_e32 v43, v43
	v_cvt_f32_i32_e32 v42, v42
	v_cvt_f32_i32_e32 v49, v49
	v_cvt_f32_i32_e32 v48, v48
	v_cvt_f32_i32_e32 v47, v47
	v_cvt_f32_i32_e32 v46, v46
	v_cvt_f32_i32_e32 v37, v37
	v_cvt_f32_i32_e32 v36, v36
	v_cvt_f32_i32_e32 v35, v35
	v_cvt_f32_i32_e32 v34, v34
	v_cvt_f32_i32_e32 v41, v41
	v_cvt_f32_i32_e32 v40, v40
	v_cvt_f32_i32_e32 v39, v39
	v_cvt_f32_i32_e32 v38, v38
	v_cvt_f32_i32_e32 v29, v29
	v_cvt_f32_i32_e32 v28, v28
	v_cvt_f32_i32_e32 v27, v27
	v_cvt_f32_i32_e32 v26, v26
	v_cvt_f32_i32_e32 v33, v33
	v_cvt_f32_i32_e32 v32, v32
	v_cvt_f32_i32_e32 v31, v31
	v_cvt_f32_i32_e32 v30, v30
	v_cvt_f32_i32_e32 v21, v21
	v_cvt_f32_i32_e32 v20, v20
	v_cvt_f32_i32_e32 v19, v19
	v_cvt_f32_i32_e32 v18, v18
	v_cvt_f32_i32_e32 v25, v25
	v_cvt_f32_i32_e32 v24, v24
	v_cvt_f32_i32_e32 v23, v23
	v_cvt_f32_i32_e32 v22, v22
	v_cvt_f32_i32_e32 v13, v13
	v_cvt_f32_i32_e32 v12, v12
	v_cvt_f32_i32_e32 v11, v11
	v_cvt_f32_i32_e32 v10, v10
	v_cvt_f32_i32_e32 v17, v17
	v_cvt_f32_i32_e32 v16, v16
	v_cvt_f32_i32_e32 v15, v15
	v_cvt_f32_i32_e32 v14, v14
	v_cvt_f32_i32_e32 v5, v5
	v_cvt_f32_i32_e32 v4, v4
	v_cvt_f32_i32_e32 v3, v3
	v_cvt_f32_i32_e32 v2, v2
	v_cvt_f32_i32_e32 v9, v9
; __device__ __forceinline__ unsigned cvt_pk_bf16(float lo, float hi) { unsigned r; asm volatile("v_cvt_pk_bf16_f32 %0, %1, %2" : "=v"(r) : "v"(lo), "v"(hi)); return r; }
;     __device__ __forceinline__ void operator()(const f32x4 (&acc)[2][2][4][2], const Unit& u, int wr, int wc, int fr, int fq) const {
;     ...
;             for (int ai = 0; ai < 2; ++ai)
; #pragma unroll
;                 for (int m = 0; m < 4; ++m) { const int row = row0 + ai * HALF + m * 16; bf16_t* rowp = O + (size_t)row * ldc + col0 + bj * HALF;
;                     f32x4 v0, v1;
;                     if constexpr (I8) { const float ra = sa[row]; const i32x4 i0 = __builtin_bit_cast(i32x4, acc[ai][bj][m][0]), i1 = __builtin_bit_cast(i32x4, acc[ai][bj][m][1]);
;                         v0 = __builtin_convertvector(i0, f32x4) * ra * s0; v1 = __builtin_convertvector(i1, f32x4) * ra * s1; }
;                     else { v0 = acc[ai][bj][m][0] * s0; v1 = acc[ai][bj][m][1] * s1; }
;                     u32x4 w; w.x = cvt_pk_bf16(v0[0], v0[1]); w.y = cvt_pk_bf16(v0[2], v0[3]); w.z = cvt_pk_bf16(v1[0], v1[1]); w.w = cvt_pk_bf16(v1[2], v1[3]);
;                     *(u32x4*)rowp = w; }
	v_cvt_f32_i32_e32 v8, v8
	v_cvt_f32_i32_e32 v7, v7
	v_cvt_f32_i32_e32 v6, v6
	s_andn2_b64 vcc, exec, s[38:39]
	s_mov_b64 s[24:25], s[34:35]
	v_pk_mul_f32 v[114:115], v[180:181], v[114:115] op_sel_hi:[0,1]
	v_pk_mul_f32 v[116:117], v[180:181], v[116:117] op_sel_hi:[0,1]
	v_pk_mul_f32 v[118:119], v[180:181], v[118:119] op_sel_hi:[0,1]
	v_pk_mul_f32 v[120:121], v[180:181], v[120:121] op_sel_hi:[0,1]
	v_pk_mul_f32 v[134:135], v[124:125], v[116:117]
	v_pk_mul_f32 v[116:117], v[122:123], v[114:115]
	v_pk_mul_f32 v[120:121], v[128:129], v[120:121]
	v_pk_mul_f32 v[118:119], v[126:127], v[118:119]
	s_nop 0
	v_cvt_pk_bf16_f32 v114, v118, v119
	v_cvt_pk_bf16_f32 v115, v120, v121
	v_cvt_pk_bf16_f32 v116, v116, v117
	v_cvt_pk_bf16_f32 v117, v134, v135
	global_store_dwordx4 v[130:131], v[114:117], off
	s_nop 1
	v_or_b32_e32 v116, 32, v152
	v_ashrrev_i32_e32 v117, 31, v116
	v_mad_i64_i32 v[114:115], s[6:7], v116, s63, v[154:155]
	v_lshl_add_u64 v[116:117], v[116:117], 2, s[46:47]
	s_nop 1
	v_lshl_add_u64 v[114:115], v[114:115], 0, v[156:157]
	v_pk_mul_f32 v[106:107], v[182:183], v[106:107] op_sel_hi:[0,1]
	v_pk_mul_f32 v[108:109], v[182:183], v[108:109] op_sel_hi:[0,1]
	v_pk_mul_f32 v[110:111], v[182:183], v[110:111] op_sel_hi:[0,1]
	v_pk_mul_f32 v[112:113], v[182:183], v[112:113] op_sel_hi:[0,1]
	v_pk_mul_f32 v[118:119], v[124:125], v[108:109]
	v_pk_mul_f32 v[108:109], v[122:123], v[106:107]
	v_pk_mul_f32 v[112:113], v[128:129], v[112:113]
	v_pk_mul_f32 v[110:111], v[126:127], v[110:111]
	s_nop 0
	v_cvt_pk_bf16_f32 v106, v110, v111
	v_cvt_pk_bf16_f32 v107, v112, v113
	v_cvt_pk_bf16_f32 v108, v108, v109
	v_cvt_pk_bf16_f32 v109, v118, v119
	global_store_dwordx4 v[114:115], v[106:109], off
	s_nop 1
	v_or_b32_e32 v108, 48, v152
	v_ashrrev_i32_e32 v109, 31, v108
	v_mad_i64_i32 v[106:107], s[6:7], v108, s63, v[154:155]
	v_lshl_add_u64 v[108:109], v[108:109], 2, s[46:47]
	s_nop 1
	v_lshl_add_u64 v[106:107], v[106:107], 0, v[156:157]
	v_pk_mul_f32 v[98:99], v[184:185], v[98:99] op_sel_hi:[0,1]
	v_pk_mul_f32 v[100:101], v[184:185], v[100:101] op_sel_hi:[0,1]
	v_pk_mul_f32 v[102:103], v[184:185], v[102:103] op_sel_hi:[0,1]
	v_pk_mul_f32 v[104:105], v[184:185], v[104:105] op_sel_hi:[0,1]
	v_pk_mul_f32 v[110:111], v[124:125], v[100:101]
	v_pk_mul_f32 v[100:101], v[122:123], v[98:99]
	v_pk_mul_f32 v[104:105], v[128:129], v[104:105]
	v_pk_mul_f32 v[102:103], v[126:127], v[102:103]
	s_nop 0
	v_cvt_pk_bf16_f32 v98, v102, v103
	v_cvt_pk_bf16_f32 v99, v104, v105
	v_cvt_pk_bf16_f32 v100, v100, v101
	v_cvt_pk_bf16_f32 v101, v110, v111
	global_store_dwordx4 v[106:107], v[98:101], off
	s_nop 1
	v_pk_mul_f32 v[90:91], v[186:187], v[90:91] op_sel_hi:[0,1]
	v_add_u32_e32 v98, 0x80, v152
	v_mad_i64_i32 v[98:99], s[6:7], v98, s63, v[154:155]
	v_pk_mul_f32 v[92:93], v[186:187], v[92:93] op_sel_hi:[0,1]
	v_lshl_add_u64 v[98:99], v[98:99], 0, v[156:157]
	v_pk_mul_f32 v[94:95], v[186:187], v[94:95] op_sel_hi:[0,1]
	v_pk_mul_f32 v[96:97], v[186:187], v[96:97] op_sel_hi:[0,1]
	v_pk_mul_f32 v[100:101], v[124:125], v[92:93]
	v_pk_mul_f32 v[92:93], v[122:123], v[90:91]
	v_pk_mul_f32 v[96:97], v[128:129], v[96:97]
	v_pk_mul_f32 v[94:95], v[126:127], v[94:95]
	s_nop 0
	v_cvt_pk_bf16_f32 v90, v94, v95
	v_cvt_pk_bf16_f32 v91, v96, v97
	v_cvt_pk_bf16_f32 v92, v92, v93
	v_cvt_pk_bf16_f32 v93, v100, v101
	global_store_dwordx4 v[98:99], v[90:93], off
	s_nop 1
	v_pk_mul_f32 v[82:83], v[188:189], v[82:83] op_sel_hi:[0,1]
	v_add_u32_e32 v90, 0x90, v152
	v_mad_i64_i32 v[90:91], s[6:7], v90, s63, v[154:155]
	v_pk_mul_f32 v[84:85], v[188:189], v[84:85] op_sel_hi:[0,1]
	v_lshl_add_u64 v[90:91], v[90:91], 0, v[156:157]
	v_pk_mul_f32 v[86:87], v[188:189], v[86:87] op_sel_hi:[0,1]
	v_pk_mul_f32 v[88:89], v[188:189], v[88:89] op_sel_hi:[0,1]
	v_pk_mul_f32 v[92:93], v[124:125], v[84:85]
	v_pk_mul_f32 v[84:85], v[122:123], v[82:83]
	v_pk_mul_f32 v[88:89], v[128:129], v[88:89]
	v_pk_mul_f32 v[86:87], v[126:127], v[86:87]
	s_nop 0
	v_cvt_pk_bf16_f32 v82, v86, v87
	v_cvt_pk_bf16_f32 v83, v88, v89
	v_cvt_pk_bf16_f32 v84, v84, v85
	v_cvt_pk_bf16_f32 v85, v92, v93
	global_store_dwordx4 v[90:91], v[82:85], off
	s_nop 1
	v_pk_mul_f32 v[74:75], v[190:191], v[74:75] op_sel_hi:[0,1]
	v_add_u32_e32 v82, 0xa0, v152
	v_mad_i64_i32 v[82:83], s[6:7], v82, s63, v[154:155]
	v_pk_mul_f32 v[76:77], v[190:191], v[76:77] op_sel_hi:[0,1]
	v_lshl_add_u64 v[82:83], v[82:83], 0, v[156:157]
	v_pk_mul_f32 v[78:79], v[190:191], v[78:79] op_sel_hi:[0,1]
	v_pk_mul_f32 v[80:81], v[190:191], v[80:81] op_sel_hi:[0,1]
	v_pk_mul_f32 v[84:85], v[124:125], v[76:77]
	v_pk_mul_f32 v[76:77], v[122:123], v[74:75]
	v_pk_mul_f32 v[80:81], v[128:129], v[80:81]
	v_pk_mul_f32 v[78:79], v[126:127], v[78:79]
	s_nop 0
	v_cvt_pk_bf16_f32 v74, v78, v79
	v_cvt_pk_bf16_f32 v75, v80, v81
	v_cvt_pk_bf16_f32 v76, v76, v77
	v_cvt_pk_bf16_f32 v77, v84, v85
	global_store_dwordx4 v[82:83], v[74:77], off
	s_nop 1
	v_pk_mul_f32 v[66:67], v[192:193], v[66:67] op_sel_hi:[0,1]
	v_add_u32_e32 v74, 0xb0, v152
	v_mad_i64_i32 v[74:75], s[6:7], v74, s63, v[154:155]
	v_pk_mul_f32 v[68:69], v[192:193], v[68:69] op_sel_hi:[0,1]
	v_lshl_add_u64 v[74:75], v[74:75], 0, v[156:157]
	v_pk_mul_f32 v[70:71], v[192:193], v[70:71] op_sel_hi:[0,1]
	v_pk_mul_f32 v[72:73], v[192:193], v[72:73] op_sel_hi:[0,1]
	v_pk_mul_f32 v[76:77], v[124:125], v[68:69]
	v_pk_mul_f32 v[68:69], v[122:123], v[66:67]
; __device__ __forceinline__ unsigned cvt_pk_bf16(float lo, float hi) { unsigned r; asm volatile("v_cvt_pk_bf16_f32 %0, %1, %2" : "=v"(r) : "v"(lo), "v"(hi)); return r; }
;     __device__ __forceinline__ void operator()(const f32x4 (&acc)[2][2][4][2], const Unit& u, int wr, int wc, int fr, int fq) const {
;     ...
;         for (int bj = 0; bj < 2; ++bj) {
;             const f32x4 s0 = *(const f32x4*)(sb + col0 + bj * HALF), s1 = *(const f32x4*)(sb + col0 + bj * HALF + 4);
; #pragma unroll
;             for (int ai = 0; ai < 2; ++ai)
; #pragma unroll
;                 for (int m = 0; m < 4; ++m) { const int row = row0 + ai * HALF + m * 16; bf16_t* rowp = O + (size_t)row * ldc + col0 + bj * HALF;
;                     f32x4 v0, v1;
;                     if constexpr (I8) { const float ra = sa[row]; const i32x4 i0 = __builtin_bit_cast(i32x4, acc[ai][bj][m][0]), i1 = __builtin_bit_cast(i32x4, acc[ai][bj][m][1]);
;                         v0 = __builtin_convertvector(i0, f32x4) * ra * s0; v1 = __builtin_convertvector(i1, f32x4) * ra * s1; }
;                     else { v0 = acc[ai][bj][m][0] * s0; v1 = acc[ai][bj][m][1] * s1; }
;                     u32x4 w; w.x = cvt_pk_bf16(v0[0], v0[1]); w.y = cvt_pk_bf16(v0[2], v0[3]); w.z = cvt_pk_bf16(v1[0], v1[1]); w.w = cvt_pk_bf16(v1[2], v1[3]);
;                     *(u32x4*)rowp = w; }
	v_pk_mul_f32 v[72:73], v[128:129], v[72:73]
	v_pk_mul_f32 v[70:71], v[126:127], v[70:71]
	s_mov_b64 s[6:7], -1
	v_cvt_pk_bf16_f32 v66, v70, v71
	v_cvt_pk_bf16_f32 v67, v72, v73
	v_cvt_pk_bf16_f32 v68, v68, v69
	v_cvt_pk_bf16_f32 v69, v76, v77
	global_store_dwordx4 v[74:75], v[66:69], off
	s_nop 0
	s_nop 1
	v_pk_mul_f32 v[58:59], v[178:179], v[58:59] op_sel_hi:[0,1]
	v_pk_mul_f32 v[60:61], v[178:179], v[60:61] op_sel_hi:[0,1]
	v_pk_mul_f32 v[62:63], v[178:179], v[62:63] op_sel_hi:[0,1]
	v_pk_mul_f32 v[64:65], v[178:179], v[64:65] op_sel_hi:[0,1]
	v_pk_mul_f32 v[76:77], v[196:197], v[60:61]
	v_pk_mul_f32 v[60:61], v[194:195], v[58:59]
	v_pk_mul_f32 v[64:65], v[200:201], v[64:65]
	v_pk_mul_f32 v[62:63], v[198:199], v[62:63]
	s_nop 0
	v_cvt_pk_bf16_f32 v58, v62, v63
	v_cvt_pk_bf16_f32 v59, v64, v65
	v_cvt_pk_bf16_f32 v60, v60, v61
	v_cvt_pk_bf16_f32 v61, v76, v77
	global_store_dwordx4 v[148:149], v[58:61], off offset:256
	s_nop 1
	v_pk_mul_f32 v[50:51], v[180:181], v[50:51] op_sel_hi:[0,1]
	v_pk_mul_f32 v[52:53], v[180:181], v[52:53] op_sel_hi:[0,1]
	v_pk_mul_f32 v[54:55], v[180:181], v[54:55] op_sel_hi:[0,1]
	v_pk_mul_f32 v[56:57], v[180:181], v[56:57] op_sel_hi:[0,1]
	v_pk_mul_f32 v[58:59], v[196:197], v[52:53]
	v_pk_mul_f32 v[52:53], v[194:195], v[50:51]
	v_pk_mul_f32 v[56:57], v[200:201], v[56:57]
	v_pk_mul_f32 v[54:55], v[198:199], v[54:55]
	s_nop 0
	v_cvt_pk_bf16_f32 v50, v54, v55
	v_cvt_pk_bf16_f32 v51, v56, v57
	v_cvt_pk_bf16_f32 v52, v52, v53
	v_cvt_pk_bf16_f32 v53, v58, v59
	global_store_dwordx4 v[130:131], v[50:53], off offset:256
	s_nop 1
	v_pk_mul_f32 v[42:43], v[182:183], v[42:43] op_sel_hi:[0,1]
	v_pk_mul_f32 v[44:45], v[182:183], v[44:45] op_sel_hi:[0,1]
	v_pk_mul_f32 v[46:47], v[182:183], v[46:47] op_sel_hi:[0,1]
	v_pk_mul_f32 v[48:49], v[182:183], v[48:49] op_sel_hi:[0,1]
	v_pk_mul_f32 v[50:51], v[196:197], v[44:45]
	v_pk_mul_f32 v[44:45], v[194:195], v[42:43]
	v_pk_mul_f32 v[48:49], v[200:201], v[48:49]
	v_pk_mul_f32 v[46:47], v[198:199], v[46:47]
	s_nop 0
	v_cvt_pk_bf16_f32 v42, v46, v47
	v_cvt_pk_bf16_f32 v43, v48, v49
	v_cvt_pk_bf16_f32 v44, v44, v45
	v_cvt_pk_bf16_f32 v45, v50, v51
	global_store_dwordx4 v[114:115], v[42:45], off offset:256
	s_nop 1
	v_pk_mul_f32 v[34:35], v[184:185], v[34:35] op_sel_hi:[0,1]
	v_pk_mul_f32 v[36:37], v[184:185], v[36:37] op_sel_hi:[0,1]
	v_pk_mul_f32 v[38:39], v[184:185], v[38:39] op_sel_hi:[0,1]
	v_pk_mul_f32 v[40:41], v[184:185], v[40:41] op_sel_hi:[0,1]
	v_pk_mul_f32 v[42:43], v[196:197], v[36:37]
	v_pk_mul_f32 v[36:37], v[194:195], v[34:35]
	v_pk_mul_f32 v[40:41], v[200:201], v[40:41]
	v_pk_mul_f32 v[38:39], v[198:199], v[38:39]
	s_nop 0
	v_cvt_pk_bf16_f32 v34, v38, v39
	v_cvt_pk_bf16_f32 v35, v40, v41
	v_cvt_pk_bf16_f32 v36, v36, v37
	v_cvt_pk_bf16_f32 v37, v42, v43
	global_store_dwordx4 v[106:107], v[34:37], off offset:256
	s_nop 1
	v_pk_mul_f32 v[26:27], v[186:187], v[26:27] op_sel_hi:[0,1]
	v_pk_mul_f32 v[28:29], v[186:187], v[28:29] op_sel_hi:[0,1]
	v_pk_mul_f32 v[30:31], v[186:187], v[30:31] op_sel_hi:[0,1]
	v_pk_mul_f32 v[32:33], v[186:187], v[32:33] op_sel_hi:[0,1]
	v_pk_mul_f32 v[34:35], v[196:197], v[28:29]
	v_pk_mul_f32 v[28:29], v[194:195], v[26:27]
	v_pk_mul_f32 v[32:33], v[200:201], v[32:33]
	v_pk_mul_f32 v[30:31], v[198:199], v[30:31]
	s_nop 0
	v_cvt_pk_bf16_f32 v26, v30, v31
	v_cvt_pk_bf16_f32 v27, v32, v33
	v_cvt_pk_bf16_f32 v28, v28, v29
	v_cvt_pk_bf16_f32 v29, v34, v35
	global_store_dwordx4 v[98:99], v[26:29], off offset:256
	s_nop 1
	v_pk_mul_f32 v[18:19], v[188:189], v[18:19] op_sel_hi:[0,1]
	v_pk_mul_f32 v[20:21], v[188:189], v[20:21] op_sel_hi:[0,1]
	v_pk_mul_f32 v[22:23], v[188:189], v[22:23] op_sel_hi:[0,1]
	v_pk_mul_f32 v[24:25], v[188:189], v[24:25] op_sel_hi:[0,1]
	v_pk_mul_f32 v[26:27], v[196:197], v[20:21]
	v_pk_mul_f32 v[20:21], v[194:195], v[18:19]
	v_pk_mul_f32 v[24:25], v[200:201], v[24:25]
	v_pk_mul_f32 v[22:23], v[198:199], v[22:23]
	s_nop 0
	v_cvt_pk_bf16_f32 v18, v22, v23
	v_cvt_pk_bf16_f32 v19, v24, v25
	v_cvt_pk_bf16_f32 v20, v20, v21
	v_cvt_pk_bf16_f32 v21, v26, v27
	global_store_dwordx4 v[90:91], v[18:21], off offset:256
	s_nop 1
	v_pk_mul_f32 v[10:11], v[190:191], v[10:11] op_sel_hi:[0,1]
	v_pk_mul_f32 v[12:13], v[190:191], v[12:13] op_sel_hi:[0,1]
	v_pk_mul_f32 v[14:15], v[190:191], v[14:15] op_sel_hi:[0,1]
	v_pk_mul_f32 v[16:17], v[190:191], v[16:17] op_sel_hi:[0,1]
	v_pk_mul_f32 v[18:19], v[196:197], v[12:13]
	v_pk_mul_f32 v[12:13], v[194:195], v[10:11]
	v_pk_mul_f32 v[16:17], v[200:201], v[16:17]
	v_pk_mul_f32 v[14:15], v[198:199], v[14:15]
	s_nop 0
	v_cvt_pk_bf16_f32 v10, v14, v15
	v_cvt_pk_bf16_f32 v11, v16, v17
	v_cvt_pk_bf16_f32 v12, v12, v13
	v_cvt_pk_bf16_f32 v13, v18, v19
	global_store_dwordx4 v[82:83], v[10:13], off offset:256
	s_nop 1
	v_pk_mul_f32 v[2:3], v[192:193], v[2:3] op_sel_hi:[0,1]
	v_pk_mul_f32 v[4:5], v[192:193], v[4:5] op_sel_hi:[0,1]
	v_pk_mul_f32 v[6:7], v[192:193], v[6:7] op_sel_hi:[0,1]
	v_pk_mul_f32 v[8:9], v[192:193], v[8:9] op_sel_hi:[0,1]
	v_pk_mul_f32 v[10:11], v[196:197], v[4:5]
	v_pk_mul_f32 v[4:5], v[194:195], v[2:3]
	v_pk_mul_f32 v[8:9], v[200:201], v[8:9]
	v_pk_mul_f32 v[6:7], v[198:199], v[6:7]
	s_nop 0
	v_cvt_pk_bf16_f32 v2, v6, v7
	v_cvt_pk_bf16_f32 v3, v8, v9
	v_cvt_pk_bf16_f32 v4, v4, v5
	v_cvt_pk_bf16_f32 v5, v10, v11
	global_store_dwordx4 v[74:75], v[2:5], off offset:256
	s_branch .Lmy_p1epi_join

; #define PG8_BAR __builtin_amdgcn_s_barrier()
;     ...
;         if constexpr (ALIGN_EPI) { if (wr == 0) PG8_BAR; }
;         if constexpr (!Epi::AFTER_DRAIN) { E(acc, cur, wr, wc, fr, fq); S.done(cur); }
;         if (!has_next) break;
; #pragma unroll
;         for (int a = 0; a < 2; ++a)
; #pragma unroll
;             for (int b = 0; b < 2; ++b)
; #pragma unroll
;                 for (int m = 0; m < 4; ++m)
; #pragma unroll
;                     for (int n = 0; n < 2; ++n) acc[a][b][m][n] = (f32x4){0.f, 0.f, 0.f, 0.f};
;         cur = nxt; cA = nA; cB = nB; ++ui;
;         if constexpr (ALIGN_EPI) { if (wr == 1) PG8_BAR; }
;     }
.Lmy_p1epi_join:
	s_cbranch_vccnz .LBB0_143
	s_andn2_b64 vcc, exec, s[0:1]
	s_cbranch_vccnz .LBB0_142
	s_barrier
	s_branch .LBB0_142
